# adds P6 router-bias load hoisted to loop top
# speedup vs baseline: 1.0016x; 1.0016x over previous
; __device__ __forceinline__ void p6_router(Ctx& X) {
;     ...
;     for (int item = X.bid; item < T / 32; item += X.G) {
;         const int tb = item * 32;
;         f32x4 acc[2][2]; float ss[2] = {0.f, 0.f};
; #pragma unroll
;         for (int a = 0; a < 2; ++a)
; #pragma unroll
;             for (int n = 0; n < 2; ++n) acc[a][n] = (f32x4){0.f, 0.f, 0.f, 0.f};
; #pragma unroll 4
;         for (int ks = 0; ks < 8; ++ks) { const int kb = 256 * w + 32 * ks + 8 * fq;
.LBB0_816:
	global_load_dwordx2 v[252:253], v[40:41], off
	s_lshl_b32 s53, s52, 5
	v_or_b32_e32 v2, s53, v104
	v_ashrrev_i32_e32 v3, 31, v2
	v_lshlrev_b64 v[18:19], 12, v[2:3]
	v_or_b32_e32 v2, 16, v2
	v_ashrrev_i32_e32 v3, 31, v2
	v_lshlrev_b64 v[20:21], 12, v[2:3]
	s_mov_b32 s8, 0
	v_mov_b32_e32 v10, 0
	v_mov_b32_e32 v11, v39
	v_mov_b32_e32 v12, v39
	v_mov_b32_e32 v13, v39
	v_mov_b32_e32 v14, 0
	v_mov_b32_e32 v15, v39
	v_mov_b32_e32 v16, v39
	v_mov_b32_e32 v17, v39
	v_mov_b32_e32 v2, 0
	v_mov_b32_e32 v3, v39
	v_mov_b32_e32 v4, v39
	v_mov_b32_e32 v5, v39
	v_mov_b32_e32 v6, 0
	v_mov_b32_e32 v7, v39
	v_mov_b32_e32 v8, v39
	v_mov_b32_e32 v9, v39
	v_mov_b32_e32 v22, 0
	v_mov_b32_e32 v23, v39

; #define LAS __attribute__((address_space(3)))
; __device__ __forceinline__ void p6_router(Ctx& X) {
;     ...
;         for (int mt = 0; mt < 2; ++mt) { float q = ss[mt]; q += __shfl_xor(q, 16); q += __shfl_xor(q, 32); if (fq == 0) ssq[w * 32 + 16 * mt + fr] = q;
; #pragma unroll
;             for (int nt = 0; nt < 2; ++nt) *(LAS f32x4*)(part + (w * 32 + 16 * mt + fr) * 32 + 16 * nt + 4 * fq) = acc[mt][nt]; }
;         __syncthreads();
;         { const int tk = tid >> 4, e0 = 2 * (tid & 15); float q = 0.f, a0 = 0.f, a1 = 0.f;
; #pragma unroll
;           for (int ww = 0; ww < 8; ++ww) { q += ssq[ww * 32 + tk]; const f32x2 p = *(const LAS f32x2*)(part + (ww * 32 + tk) * 32 + e0); a0 += p.x; a1 += p.y; }
;           const float rstd = rsqrtf(q * (1.f / D) + EPS);
;           lgt[tk * 32 + e0] = a0 * rstd + XP_b_router(X)[e0]; lgt[tk * 32 + e0 + 1] = a1 * rstd + XP_b_router(X)[e0 + 1];
;           if ((tid & 15) == 0) rs[tk] = rstd; }
;         __syncthreads();
.LBB0_822:
	s_or_b64 exec, exec, s[8:9]
	ds_write_b128 v122, v[2:5] offset:2048
	ds_write_b128 v122, v[6:9] offset:2112
	s_waitcnt lgkmcnt(0)
	s_barrier
	v_add_u32_e32 v8, 0x8000, v123
	ds_read2_b32 v[2:3], v8 offset1:32
	ds_read2_b32 v[6:7], v8 offset0:64 offset1:96
	v_add_u32_e32 v9, v107, v108
	s_waitcnt lgkmcnt(1)
	v_add_f32_e32 v2, 0, v2
	v_add_f32_e32 v2, v2, v3
	s_waitcnt lgkmcnt(0)
	v_add_f32_e32 v2, v2, v6
	v_add_f32_e32 v16, v2, v7
	ds_read2_b32 v[2:3], v8 offset0:128 offset1:160
	ds_read2_b32 v[6:7], v8 offset0:192 offset1:224
	ds_read_b64 v[8:9], v9
	ds_read_b64 v[10:11], v112
	ds_read_b64 v[12:13], v113
	ds_read_b64 v[14:15], v114
	s_waitcnt lgkmcnt(5)
	v_add_f32_e32 v2, v16, v2
	v_add_f32_e32 v2, v2, v3
	s_waitcnt lgkmcnt(4)
	v_add_f32_e32 v2, v2, v6
	v_add_f32_e32 v2, v2, v7
	v_fmamk_f32 v2, v2, 0x3a000000, v119
	v_mul_f32_e32 v3, 0x4b800000, v2
	v_cmp_gt_f32_e32 vcc, s50, v2
	s_waitcnt lgkmcnt(3)
	v_pk_add_f32 v[8:9], v[8:9], 0 op_sel_hi:[1,0]
	ds_read_b64 v[6:7], v115
	ds_read_b64 v[16:17], v116
	ds_read_b64 v[18:19], v117
	ds_read_b64 v[20:21], v118
	v_cndmask_b32_e32 v2, v2, v3, vcc
	s_waitcnt lgkmcnt(6)
	v_pk_add_f32 v[8:9], v[8:9], v[10:11]
	v_rsq_f32_e32 v2, v2
	s_waitcnt lgkmcnt(5)
	v_pk_add_f32 v[8:9], v[8:9], v[12:13]
	v_mul_f32_e32 v3, 0x45800000, v2
	s_waitcnt lgkmcnt(4)
	v_pk_add_f32 v[8:9], v[8:9], v[14:15]
	v_cndmask_b32_e32 v2, v2, v3, vcc
	s_waitcnt lgkmcnt(3)
	v_pk_add_f32 v[6:7], v[8:9], v[6:7]
	s_waitcnt lgkmcnt(2)
	v_pk_add_f32 v[6:7], v[6:7], v[16:17]
	s_waitcnt lgkmcnt(1)
	v_pk_add_f32 v[6:7], v[6:7], v[18:19]
	s_waitcnt lgkmcnt(0)
	v_pk_add_f32 v[6:7], v[6:7], v[20:21]
	s_waitcnt vmcnt(0)
	v_pk_fma_f32 v[4:5], v[6:7], v[2:3], v[252:253] op_sel_hi:[1,0,1]
	ds_write_b64 v109, v[4:5] offset:33792
	s_and_saveexec_b64 s[8:9], s[4:5]
	ds_write_b32 v123, v2 offset:37888
	s_or_b64 exec, exec, s[8:9]
	s_waitcnt lgkmcnt(0)
	s_barrier
	s_and_saveexec_b64 s[44:45], s[6:7]
	s_cbranch_execz .LBB0_815
	v_mov_b32_e32 v4, 0xff61b1e6
	s_mov_b32 s8, 0
	v_mov_b32_e32 v2, 0
	v_mov_b32_e32 v3, v111

; #define LAS __attribute__((address_space(3)))
;     __device__ __forceinline__ bool next(int i, pg8::Unit& u) const {
;         const int NB = __builtin_amdgcn_readfirstlane(tab[0]); const int L = i * G + c; if (L >= NB * nN) return false;
;         const int b = L / nN, pn = L - b * nN, e = __builtin_amdgcn_readfirstlane(tab[64 + b]);
;         u.pa = A; u.pb = B + (size_t)e * bexp + (size_t)pn * 256 * 128; u.row0 = b * 256; u.col0 = pn * 256; u.aux = e; u.blk = b; return true;
;     }
; __device__ __forceinline__ void moe_tables(Ctx& X) {
;     LAS int* tab = (LAS int*)(X.lds + LDS_TAB);
;     if (X.tid < 64) { const int e = X.tid;
;         const int cnt = (e < NE) ? (int)__hip_atomic_load(XP_ctl(X) + CW_CNT + 64 * e, __ATOMIC_RELAXED, __HIP_MEMORY_SCOPE_AGENT) : 0; const int k = (cnt + 255) >> 8;
;         int incl = k;
; #pragma unroll
;         for (int o = 1; o < 64; o <<= 1) { const int t = __shfl_up(incl, o); if (e >= o) incl += t; }
;         const int first = incl - k;
;         if (e < NE) { tab[8 + e] = first; for (int b = 0; b < k; ++b) { if (first + b < MAXBLK) { tab[64 + first + b] = e; tab[256 + first + b] = (cnt - 256 * b) < 256 ? (cnt - 256 * b) : 256; } } }
;         if (e == NE - 1) { tab[8 + NE] = incl; tab[0] = incl < MAXBLK ? incl : MAXBLK; } }
;     __syncthreads();
.LBB0_1022:
	s_cmp_lg_u32 s93, 0
	s_cbranch_scc1 .Lsch8_done
	s_and_b32 s98, s87, 7
	s_lshl_b32 s98, s98, 2
	s_lshr_b32 s100, s87, 6
	s_or_b32 s98, s98, s100
	s_bfe_u32 s101, s87, 0x30003
	s_lshr_b32 s99, s98, 2
	s_and_b32 s100, s98, 3
	s_lshl_b32 s100, s100, 3
	s_or_b32 s99, s99, s100
	v_and_b32_e32 v2, 63, v0
	v_lshlrev_b32_e32 v3, 2, v2
	v_add_u32_e32 v3, 0x23c00, v3
	v_mov_b32_e32 v4, 0x7fff0000
	ds_write_b32 v3, v4
	v_min_u32_e32 v5, 31, v2
	v_lshlrev_b32_e32 v5, 2, v5
	v_add_u32_e32 v5, 0x22020, v5
	ds_read2_b32 v[6:7], v5 offset1:1
	s_waitcnt lgkmcnt(0)
	v_sub_u32_e32 v8, v7, v6
	v_add_u32_e32 v9, -1, v7
	v_max_i32_e32 v9, 0, v9
	v_lshlrev_b32_e32 v9, 2, v9
	v_add_u32_e32 v9, 0x22400, v9
	ds_read_b32 v9, v9
	s_waitcnt lgkmcnt(0)
	v_cmp_gt_i32_e32 vcc, 0x81, v9
	v_cmp_lt_i32_e64 s[10:11], 0, v8
	s_and_b64 vcc, vcc, s[10:11]
	v_cmp_gt_u32_e64 s[10:11], 32, v2
	s_and_b64 vcc, vcc, s[10:11]
	v_cndmask_b32_e64 v10, 0, 1, vcc
	v_cndmask_b32_e64 v8, 0, v8, s[10:11]
	v_sub_u32_e32 v11, v8, v10
	v_lshl_or_b32 v13, v10, 16, v11
	s_nop 1
	v_add_u32_dpp v13, v13, v13 row_shr:1 row_mask:0xf bank_mask:0xf bound_ctrl:0
	s_nop 1
	v_add_u32_dpp v13, v13, v13 row_shr:2 row_mask:0xf bank_mask:0xf bound_ctrl:0
	s_nop 1
	v_add_u32_dpp v13, v13, v13 row_shr:4 row_mask:0xf bank_mask:0xf bound_ctrl:0
	s_nop 1
	v_add_u32_dpp v13, v13, v13 row_shr:8 row_mask:0xf bank_mask:0xf bound_ctrl:0
	s_nop 1
	v_add_u32_dpp v13, v13, v13 row_bcast:15 row_mask:0xa bank_mask:0xf
	s_nop 1
	v_and_b32_e32 v14, 0xffff, v13
	v_sub_u32_e32 v14, v14, v11
	v_lshrrev_b32_e32 v15, 16, v13
	v_sub_u32_e32 v15, v15, v10
	v_add_u32_e32 v16, v14, v11
	v_add_u32_e32 v17, -1, v8
	v_mov_b32_e32 v18, v15
	s_mov_b32 s12, 0
	s_mov_b64 s[8:9], exec
